# loop-edge edit: NSA tile-loop head mask test reuses the SCC of the scalar and (on v18)
# baseline (speedup 1.0000x reference)
.LBB0_2436:
	s_and_b64 vcc, s[78:79], exec
	s_nop 0
	s_nop 0
	s_nop 0
	s_cselect_b64 s[80:81], -1, 0
	s_and_b32 s82, s2, 0x6000
	v_add_u32_e32 v224, s82, v182
	ds_read_b128 v[228:231], v224 offset:512
	ds_read_b128 v[232:235], v224 offset:2560
	ds_read_b128 v[236:239], v224 offset:4608
	ds_read_b128 v[240:243], v224 offset:6656
	s_waitcnt lgkmcnt(3)
	v_mfma_f32_32x32x16_bf16 v[82:97], v[228:231], v[114:117], v[34:49]
	s_waitcnt lgkmcnt(2)
	v_mfma_f32_32x32x16_bf16 v[82:97], v[232:235], v[118:121], v[82:97]
	s_waitcnt lgkmcnt(1)
	v_mfma_f32_32x32x16_bf16 v[82:97], v[236:239], v[122:125], v[82:97]
	s_waitcnt lgkmcnt(0)
	v_mfma_f32_32x32x16_bf16 v[82:97], v[240:243], v[126:129], v[82:97]
	ds_read_b64_tr_b16 v[228:229], v225
	ds_read_b64_tr_b16 v[230:231], v225 offset:512
	ds_read_b64_tr_b16 v[232:233], v225 offset:1024
	ds_read_b64_tr_b16 v[234:235], v225 offset:1536
	ds_read_b64_tr_b16 v[236:237], v225 offset:4096
	ds_read_b64_tr_b16 v[238:239], v225 offset:4608
	ds_read_b64_tr_b16 v[240:241], v225 offset:5120
	ds_read_b64_tr_b16 v[242:243], v225 offset:5632
	s_cbranch_vccz .LBB0_2438
	v_cndmask_b32_e64 v50, v50, v1, s[78:79]
	v_cndmask_b32_e64 v51, v51, v1, s[78:79]
	v_cndmask_b32_e64 v52, v52, v1, s[78:79]
	v_cndmask_b32_e64 v53, v53, v1, s[78:79]
	v_cndmask_b32_e64 v54, v54, v1, s[78:79]
	v_cndmask_b32_e64 v55, v55, v1, s[78:79]
	v_cndmask_b32_e64 v56, v56, v1, s[78:79]
	v_cndmask_b32_e64 v57, v57, v1, s[78:79]
	v_cndmask_b32_e64 v58, v58, v1, s[78:79]
	v_cndmask_b32_e64 v59, v59, v1, s[78:79]
	v_cndmask_b32_e64 v60, v60, v1, s[78:79]
	v_cndmask_b32_e64 v61, v61, v1, s[78:79]
	v_cndmask_b32_e64 v62, v62, v1, s[78:79]
	v_cndmask_b32_e64 v63, v63, v1, s[78:79]
	v_cndmask_b32_e64 v64, v64, v1, s[78:79]
	v_cndmask_b32_e64 v65, v65, v1, s[78:79]
